# previous + MoE GEMM1 SwiGLU epilogue re-emitted with the 8 elements of a row in lock-step (no dependent per-element chains, no trans-hazard nops)
# speedup vs baseline: 1.0130x; 1.0047x over previous
; #define LAS __attribute__((address_space(3)))
; __device__ __forceinline__ unsigned pk4_fp8(float a, float b, float c, float d) { int w = 0; w = __builtin_amdgcn_cvt_pk_fp8_f32(a, b, w, false); w = __builtin_amdgcn_cvt_pk_fp8_f32(c, d, w, true); return (unsigned)w; }
;     __device__ __forceinline__ void operator()(const Acc& acc, const Unit& u, int wr, int wc, int fr, int fq) const {
;         const int row0 = u.pm * 256 + wr * 64 + fr, a0 = u.pn * 128 + wc * 32 + 8 * fq; const LAS float* b1 = bias_lds + (u.ui < 18 ? u.ui : 0) * 256 + 2 * (wc * 32 + 8 * fq); bf16_t* dst = WSP(bf16_t, dst_off);
;         float bg[8], bl[8];
; #pragma unroll
;         for (int q = 0; q < 4; ++q) { const f32x4 t = *(const LAS f32x4*)(b1 + 4 * q); bg[2 * q] = t[0]; bl[2 * q] = t[1] + 1.f; bg[2 * q + 1] = t[2]; bl[2 * q + 1] = t[3] + 1.f; }
; #pragma unroll
;         for (int ai = 0; ai < 2; ++ai)
; #pragma unroll
;             for (int m = 0; m < 4; ++m) { const int row = row0 + ai * 128 + m * 16; float o[8];
; #pragma unroll
;                 for (int j = 0; j < 8; ++j) { float g = acc[ai][0][m][j >> 2][j & 3] * (MOE1_FP6 ? 1.f : W8_INV) + bg[j], l = acc[ai][1][m][j >> 2][j & 3] * (MOE1_FP6 ? 1.f : W8_INV) + bl[j];
;                     g = fminf(g, 7.f); l = fminf(fmaxf(l, -6.f), 8.f);
;                     o[j] = g * __builtin_amdgcn_rcpf(1.f + __builtin_amdgcn_exp2f(-2.4554669595930156f * g)) * l; }
;                 if (MOE_FP8) { u32x2 w; w.x = pk4_fp8(o[0], o[1], o[2], o[3]); w.y = pk4_fp8(o[4], o[5], o[6], o[7]); *(u32x2*)((unsigned char*)dst + (size_t)row * DE + a0) = w; }
.LBB0_2002:
	s_lshl_b32 s2, s50, 8
	s_cmp_lt_i32 s50, 18
	s_cselect_b32 s2, s2, 0
	v_lshl_add_u32 v2, s2, 2, v225
	ds_read_b128 v[14:17], v2
	ds_read_b128 v[10:13], v2 offset:16
	ds_read_b128 v[6:9], v2 offset:32
	ds_read_b128 v[2:5], v2 offset:48
	v_lshl_or_b32 v18, s44, 7, v224
	v_ashrrev_i32_e32 v19, 31, v18
	v_lshl_add_u64 v[20:21], s[14:15], 0, v[18:19]
	v_lshl_add_u32 v22, s43, 8, v223
	v_ashrrev_i32_e32 v23, 31, v22
	v_lshlrev_b64 v[18:19], 11, v[22:23]
	v_lshl_add_u64 v[18:19], v[20:21], 0, v[18:19]
	s_waitcnt lgkmcnt(0)
	v_add_f32_e32 v15, 1.0, v15
	v_add_f32_e32 v17, 1.0, v17
	v_add_f32_e32 v11, 1.0, v11
	v_add_f32_e32 v13, 1.0, v13
	v_add_f32_e32 v7, 1.0, v7
	v_add_f32_e32 v9, 1.0, v9
	v_add_f32_e32 v3, 1.0, v3
	v_add_f32_e32 v5, 1.0, v5
	v_add_f32_e32 v232, v178, v14
	v_add_f32_e32 v233, v179, v16
	v_add_f32_e32 v234, v180, v10
	v_add_f32_e32 v235, v181, v12
	v_add_f32_e32 v236, v174, v6
	v_add_f32_e32 v237, v175, v8
	v_add_f32_e32 v238, v176, v2
	v_add_f32_e32 v239, v177, v4
	v_min_f32_e32 v232, 0x40e00000, v232
	v_min_f32_e32 v233, 0x40e00000, v233
	v_min_f32_e32 v234, 0x40e00000, v234
	v_min_f32_e32 v235, 0x40e00000, v235
	v_min_f32_e32 v236, 0x40e00000, v236
	v_min_f32_e32 v237, 0x40e00000, v237
	v_min_f32_e32 v238, 0x40e00000, v238
	v_min_f32_e32 v239, 0x40e00000, v239
	v_mul_f32_e32 v243, 0xc01d265f, v232
	v_mul_f32_e32 v244, 0xc01d265f, v233
	v_mul_f32_e32 v245, 0xc01d265f, v234
	v_mul_f32_e32 v246, 0xc01d265f, v235
	v_mul_f32_e32 v247, 0xc01d265f, v236
	v_mul_f32_e32 v248, 0xc01d265f, v237
	v_mul_f32_e32 v249, 0xc01d265f, v238
	v_mul_f32_e32 v250, 0xc01d265f, v239
	v_exp_f32_e32 v243, v243
	v_exp_f32_e32 v244, v244
	v_exp_f32_e32 v245, v245
	v_exp_f32_e32 v246, v246
	v_exp_f32_e32 v247, v247
	v_exp_f32_e32 v248, v248
	v_exp_f32_e32 v249, v249
	v_exp_f32_e32 v250, v250
	v_add_f32_e32 v202, v146, v15
	v_add_f32_e32 v203, v147, v17
	v_add_f32_e32 v204, v148, v11
	v_add_f32_e32 v205, v149, v13
	v_add_f32_e32 v206, v142, v7
	v_add_f32_e32 v207, v143, v9
	v_add_f32_e32 v208, v144, v3
	v_add_f32_e32 v209, v145, v5
	v_med3_f32 v202, v202, s86, v228
	v_med3_f32 v203, v203, s86, v228
	v_med3_f32 v204, v204, s86, v228
	v_med3_f32 v205, v205, s86, v228
	v_med3_f32 v206, v206, s86, v228
	v_med3_f32 v207, v207, s86, v228
	v_med3_f32 v208, v208, s86, v228
	v_med3_f32 v209, v209, s86, v228
	v_add_f32_e32 v243, 1.0, v243
	v_add_f32_e32 v244, 1.0, v244
	v_add_f32_e32 v245, 1.0, v245
	v_add_f32_e32 v246, 1.0, v246
	v_add_f32_e32 v247, 1.0, v247
	v_add_f32_e32 v248, 1.0, v248
	v_add_f32_e32 v249, 1.0, v249
	v_add_f32_e32 v250, 1.0, v250
	v_rcp_f32_e32 v243, v243
	v_rcp_f32_e32 v244, v244
	v_rcp_f32_e32 v245, v245
	v_rcp_f32_e32 v246, v246
	v_rcp_f32_e32 v247, v247
	v_rcp_f32_e32 v248, v248
	v_rcp_f32_e32 v249, v249
	v_rcp_f32_e32 v250, v250
	v_mul_f32_e32 v232, v232, v243
	v_mul_f32_e32 v233, v233, v244
	v_mul_f32_e32 v234, v234, v245
	v_mul_f32_e32 v235, v235, v246
	v_mul_f32_e32 v236, v236, v247
	v_mul_f32_e32 v237, v237, v248
	v_mul_f32_e32 v238, v238, v249
	v_mul_f32_e32 v239, v239, v250
	v_mul_f32_e32 v232, v202, v232
	v_mul_f32_e32 v233, v203, v233
	v_mul_f32_e32 v234, v204, v234
	v_mul_f32_e32 v235, v205, v235
	v_mul_f32_e32 v236, v206, v236
	v_mul_f32_e32 v237, v207, v237
	v_mul_f32_e32 v238, v208, v238
	v_mul_f32_e32 v239, v209, v239
	v_mov_b32_e32 v210, 0
	v_mov_b32_e32 v211, 0
	v_cvt_pk_fp8_f32 v210, v232, v233
	v_cvt_pk_fp8_f32 v211, v236, v237
	v_cvt_pk_fp8_f32 v210, v234, v235 op_sel:[0,0,1]
	v_cvt_pk_fp8_f32 v211, v238, v239 op_sel:[0,0,1]
	s_nop 0
	global_store_dwordx2 v[18:19], v[210:211], off
	v_add_f32_e32 v232, v170, v14
	v_add_f32_e32 v233, v171, v16
	v_add_f32_e32 v234, v172, v10
	v_add_f32_e32 v235, v173, v12
	v_add_f32_e32 v236, v166, v6
	v_add_f32_e32 v237, v167, v8
	v_add_f32_e32 v238, v168, v2
	v_add_f32_e32 v239, v169, v4
	v_min_f32_e32 v232, 0x40e00000, v232
	v_min_f32_e32 v233, 0x40e00000, v233
	v_min_f32_e32 v234, 0x40e00000, v234
	v_min_f32_e32 v235, 0x40e00000, v235
	v_min_f32_e32 v236, 0x40e00000, v236
	v_min_f32_e32 v237, 0x40e00000, v237
	v_min_f32_e32 v238, 0x40e00000, v238
	v_min_f32_e32 v239, 0x40e00000, v239
	v_mul_f32_e32 v243, 0xc01d265f, v232
	v_mul_f32_e32 v244, 0xc01d265f, v233
	v_mul_f32_e32 v245, 0xc01d265f, v234
	v_mul_f32_e32 v246, 0xc01d265f, v235
	v_mul_f32_e32 v247, 0xc01d265f, v236
	v_mul_f32_e32 v248, 0xc01d265f, v237
	v_mul_f32_e32 v249, 0xc01d265f, v238
	v_mul_f32_e32 v250, 0xc01d265f, v239
	v_exp_f32_e32 v243, v243
	v_exp_f32_e32 v244, v244
	v_exp_f32_e32 v245, v245
	v_exp_f32_e32 v246, v246
	v_exp_f32_e32 v247, v247
	v_exp_f32_e32 v248, v248
	v_exp_f32_e32 v249, v249
	v_exp_f32_e32 v250, v250
	v_add_f32_e32 v202, v138, v15
	v_add_f32_e32 v203, v139, v17
	v_add_f32_e32 v204, v140, v11
	v_add_f32_e32 v205, v141, v13
	v_add_f32_e32 v206, v134, v7
	v_add_f32_e32 v207, v135, v9
	v_add_f32_e32 v208, v136, v3
	v_add_f32_e32 v209, v137, v5
	v_med3_f32 v202, v202, s86, v228
	v_med3_f32 v203, v203, s86, v228
	v_med3_f32 v204, v204, s86, v228
	v_med3_f32 v205, v205, s86, v228
	v_med3_f32 v206, v206, s86, v228
	v_med3_f32 v207, v207, s86, v228
	v_med3_f32 v208, v208, s86, v228
	v_med3_f32 v209, v209, s86, v228
	v_add_f32_e32 v243, 1.0, v243
	v_add_f32_e32 v244, 1.0, v244
	v_add_f32_e32 v245, 1.0, v245
	v_add_f32_e32 v246, 1.0, v246
	v_add_f32_e32 v247, 1.0, v247
	v_add_f32_e32 v248, 1.0, v248
	v_add_f32_e32 v249, 1.0, v249
	v_add_f32_e32 v250, 1.0, v250
	v_rcp_f32_e32 v243, v243
	v_rcp_f32_e32 v244, v244
	v_rcp_f32_e32 v245, v245
	v_rcp_f32_e32 v246, v246
	v_rcp_f32_e32 v247, v247
	v_rcp_f32_e32 v248, v248
	v_rcp_f32_e32 v249, v249
	v_rcp_f32_e32 v250, v250
	v_mul_f32_e32 v232, v232, v243
; __device__ __forceinline__ unsigned pk4_fp8(float a, float b, float c, float d) { int w = 0; w = __builtin_amdgcn_cvt_pk_fp8_f32(a, b, w, false); w = __builtin_amdgcn_cvt_pk_fp8_f32(c, d, w, true); return (unsigned)w; }
;     __device__ __forceinline__ void operator()(const Acc& acc, const Unit& u, int wr, int wc, int fr, int fq) const {
;     ...
;             for (int m = 0; m < 4; ++m) { const int row = row0 + ai * 128 + m * 16; float o[8];
; #pragma unroll
;                 for (int j = 0; j < 8; ++j) { float g = acc[ai][0][m][j >> 2][j & 3] * (MOE1_FP6 ? 1.f : W8_INV) + bg[j], l = acc[ai][1][m][j >> 2][j & 3] * (MOE1_FP6 ? 1.f : W8_INV) + bl[j];
;                     g = fminf(g, 7.f); l = fminf(fmaxf(l, -6.f), 8.f);
;                     o[j] = g * __builtin_amdgcn_rcpf(1.f + __builtin_amdgcn_exp2f(-2.4554669595930156f * g)) * l; }
;                 if (MOE_FP8) { u32x2 w; w.x = pk4_fp8(o[0], o[1], o[2], o[3]); w.y = pk4_fp8(o[4], o[5], o[6], o[7]); *(u32x2*)((unsigned char*)dst + (size_t)row * DE + a0) = w; }
	v_mul_f32_e32 v233, v233, v244
	v_mul_f32_e32 v234, v234, v245
	v_mul_f32_e32 v235, v235, v246
	v_mul_f32_e32 v236, v236, v247
	v_mul_f32_e32 v237, v237, v248
	v_mul_f32_e32 v238, v238, v249
	v_mul_f32_e32 v239, v239, v250
	v_mul_f32_e32 v232, v202, v232
	v_mul_f32_e32 v233, v203, v233
	v_mul_f32_e32 v234, v204, v234
	v_mul_f32_e32 v235, v205, v235
	v_mul_f32_e32 v236, v206, v236
	v_mul_f32_e32 v237, v207, v237
	v_mul_f32_e32 v238, v208, v238
	v_mul_f32_e32 v239, v209, v239
	v_mov_b32_e32 v212, 0
	v_mov_b32_e32 v213, 0
	v_cvt_pk_fp8_f32 v212, v232, v233
	v_cvt_pk_fp8_f32 v213, v236, v237
	v_cvt_pk_fp8_f32 v212, v234, v235 op_sel:[0,0,1]
	v_cvt_pk_fp8_f32 v213, v238, v239 op_sel:[0,0,1]
	v_add_co_u32_e32 v24, vcc, 0x8000, v18
	s_nop 1
	v_addc_co_u32_e32 v25, vcc, 0, v19, vcc
	global_store_dwordx2 v[24:25], v[212:213], off
	v_add_f32_e32 v232, v162, v14
	v_add_f32_e32 v233, v163, v16
	v_add_f32_e32 v234, v164, v10
	v_add_f32_e32 v235, v165, v12
	v_add_f32_e32 v236, v158, v6
	v_add_f32_e32 v237, v159, v8
	v_add_f32_e32 v238, v160, v2
	v_add_f32_e32 v239, v161, v4
	v_min_f32_e32 v232, 0x40e00000, v232
	v_min_f32_e32 v233, 0x40e00000, v233
	v_min_f32_e32 v234, 0x40e00000, v234
	v_min_f32_e32 v235, 0x40e00000, v235
	v_min_f32_e32 v236, 0x40e00000, v236
	v_min_f32_e32 v237, 0x40e00000, v237
	v_min_f32_e32 v238, 0x40e00000, v238
	v_min_f32_e32 v239, 0x40e00000, v239
	v_mul_f32_e32 v243, 0xc01d265f, v232
	v_mul_f32_e32 v244, 0xc01d265f, v233
	v_mul_f32_e32 v245, 0xc01d265f, v234
	v_mul_f32_e32 v246, 0xc01d265f, v235
	v_mul_f32_e32 v247, 0xc01d265f, v236
	v_mul_f32_e32 v248, 0xc01d265f, v237
	v_mul_f32_e32 v249, 0xc01d265f, v238
	v_mul_f32_e32 v250, 0xc01d265f, v239
	v_exp_f32_e32 v243, v243
	v_exp_f32_e32 v244, v244
	v_exp_f32_e32 v245, v245
	v_exp_f32_e32 v246, v246
	v_exp_f32_e32 v247, v247
	v_exp_f32_e32 v248, v248
	v_exp_f32_e32 v249, v249
	v_exp_f32_e32 v250, v250
	v_add_f32_e32 v202, v130, v15
	v_add_f32_e32 v203, v131, v17
	v_add_f32_e32 v204, v132, v11
	v_add_f32_e32 v205, v133, v13
	v_add_f32_e32 v206, v126, v7
	v_add_f32_e32 v207, v127, v9
	v_add_f32_e32 v208, v128, v3
	v_add_f32_e32 v209, v129, v5
	v_med3_f32 v202, v202, s86, v228
	v_med3_f32 v203, v203, s86, v228
	v_med3_f32 v204, v204, s86, v228
	v_med3_f32 v205, v205, s86, v228
	v_med3_f32 v206, v206, s86, v228
	v_med3_f32 v207, v207, s86, v228
	v_med3_f32 v208, v208, s86, v228
	v_med3_f32 v209, v209, s86, v228
	v_add_f32_e32 v243, 1.0, v243
	v_add_f32_e32 v244, 1.0, v244
	v_add_f32_e32 v245, 1.0, v245
	v_add_f32_e32 v246, 1.0, v246
	v_add_f32_e32 v247, 1.0, v247
	v_add_f32_e32 v248, 1.0, v248
	v_add_f32_e32 v249, 1.0, v249
	v_add_f32_e32 v250, 1.0, v250
	v_rcp_f32_e32 v243, v243
	v_rcp_f32_e32 v244, v244
	v_rcp_f32_e32 v245, v245
	v_rcp_f32_e32 v246, v246
	v_rcp_f32_e32 v247, v247
	v_rcp_f32_e32 v248, v248
	v_rcp_f32_e32 v249, v249
	v_rcp_f32_e32 v250, v250
	v_mul_f32_e32 v232, v232, v243
	v_mul_f32_e32 v233, v233, v244
	v_mul_f32_e32 v234, v234, v245
	v_mul_f32_e32 v235, v235, v246
	v_mul_f32_e32 v236, v236, v247
	v_mul_f32_e32 v237, v237, v248
	v_mul_f32_e32 v238, v238, v249
	v_mul_f32_e32 v239, v239, v250
	v_mul_f32_e32 v232, v202, v232
	v_mul_f32_e32 v233, v203, v233
	v_mul_f32_e32 v234, v204, v234
	v_mul_f32_e32 v235, v205, v235
	v_mul_f32_e32 v236, v206, v236
	v_mul_f32_e32 v237, v207, v237
	v_mul_f32_e32 v238, v208, v238
	v_mul_f32_e32 v239, v209, v239
	v_mov_b32_e32 v210, 0
	v_mov_b32_e32 v211, 0
	v_cvt_pk_fp8_f32 v210, v232, v233
	v_cvt_pk_fp8_f32 v211, v236, v237
	v_cvt_pk_fp8_f32 v210, v234, v235 op_sel:[0,0,1]
	v_cvt_pk_fp8_f32 v211, v238, v239 op_sel:[0,0,1]
	v_add_co_u32_e32 v24, vcc, 0x10000, v18
	s_nop 1
	v_addc_co_u32_e32 v25, vcc, 0, v19, vcc
	global_store_dwordx2 v[24:25], v[210:211], off
	v_add_f32_e32 v232, v154, v14
	v_add_f32_e32 v233, v155, v16
	v_add_f32_e32 v234, v156, v10
	v_add_f32_e32 v235, v157, v12
	v_add_f32_e32 v236, v150, v6
	v_add_f32_e32 v237, v151, v8
	v_add_f32_e32 v238, v152, v2
	v_add_f32_e32 v239, v153, v4
	v_min_f32_e32 v232, 0x40e00000, v232
	v_min_f32_e32 v233, 0x40e00000, v233
	v_min_f32_e32 v234, 0x40e00000, v234
	v_min_f32_e32 v235, 0x40e00000, v235
	v_min_f32_e32 v236, 0x40e00000, v236
	v_min_f32_e32 v237, 0x40e00000, v237
	v_min_f32_e32 v238, 0x40e00000, v238
	v_min_f32_e32 v239, 0x40e00000, v239
	v_mul_f32_e32 v243, 0xc01d265f, v232
	v_mul_f32_e32 v244, 0xc01d265f, v233
	v_mul_f32_e32 v245, 0xc01d265f, v234
	v_mul_f32_e32 v246, 0xc01d265f, v235
	v_mul_f32_e32 v247, 0xc01d265f, v236
	v_mul_f32_e32 v248, 0xc01d265f, v237
	v_mul_f32_e32 v249, 0xc01d265f, v238
	v_mul_f32_e32 v250, 0xc01d265f, v239
	v_exp_f32_e32 v243, v243
	v_exp_f32_e32 v244, v244
	v_exp_f32_e32 v245, v245
	v_exp_f32_e32 v246, v246
	v_exp_f32_e32 v247, v247
	v_exp_f32_e32 v248, v248
	v_exp_f32_e32 v249, v249
	v_exp_f32_e32 v250, v250
	v_add_f32_e32 v202, v122, v15
	v_add_f32_e32 v203, v123, v17
	v_add_f32_e32 v204, v124, v11
	v_add_f32_e32 v205, v125, v13
	v_add_f32_e32 v206, v118, v7
	v_add_f32_e32 v207, v119, v9
	v_add_f32_e32 v208, v120, v3
	v_add_f32_e32 v209, v121, v5
	v_med3_f32 v202, v202, s86, v228
	v_med3_f32 v203, v203, s86, v228
	v_med3_f32 v204, v204, s86, v228
	v_med3_f32 v205, v205, s86, v228
	v_med3_f32 v206, v206, s86, v228
	v_med3_f32 v207, v207, s86, v228
	v_med3_f32 v208, v208, s86, v228
	v_med3_f32 v209, v209, s86, v228
	v_add_f32_e32 v243, 1.0, v243
	v_add_f32_e32 v244, 1.0, v244
	v_add_f32_e32 v245, 1.0, v245
	v_add_f32_e32 v246, 1.0, v246
	v_add_f32_e32 v247, 1.0, v247
	v_add_f32_e32 v248, 1.0, v248
	v_add_f32_e32 v249, 1.0, v249
	v_add_f32_e32 v250, 1.0, v250
	v_rcp_f32_e32 v243, v243
	v_rcp_f32_e32 v244, v244
	v_rcp_f32_e32 v245, v245
; __device__ __forceinline__ unsigned pk4_fp8(float a, float b, float c, float d) { int w = 0; w = __builtin_amdgcn_cvt_pk_fp8_f32(a, b, w, false); w = __builtin_amdgcn_cvt_pk_fp8_f32(c, d, w, true); return (unsigned)w; }
;     __device__ __forceinline__ void operator()(const Acc& acc, const Unit& u, int wr, int wc, int fr, int fq) const {
;     ...
;             for (int m = 0; m < 4; ++m) { const int row = row0 + ai * 128 + m * 16; float o[8];
; #pragma unroll
;                 for (int j = 0; j < 8; ++j) { float g = acc[ai][0][m][j >> 2][j & 3] * (MOE1_FP6 ? 1.f : W8_INV) + bg[j], l = acc[ai][1][m][j >> 2][j & 3] * (MOE1_FP6 ? 1.f : W8_INV) + bl[j];
;                     g = fminf(g, 7.f); l = fminf(fmaxf(l, -6.f), 8.f);
;                     o[j] = g * __builtin_amdgcn_rcpf(1.f + __builtin_amdgcn_exp2f(-2.4554669595930156f * g)) * l; }
;                 if (MOE_FP8) { u32x2 w; w.x = pk4_fp8(o[0], o[1], o[2], o[3]); w.y = pk4_fp8(o[4], o[5], o[6], o[7]); *(u32x2*)((unsigned char*)dst + (size_t)row * DE + a0) = w; }
	v_rcp_f32_e32 v246, v246
	v_rcp_f32_e32 v247, v247
	v_rcp_f32_e32 v248, v248
	v_rcp_f32_e32 v249, v249
	v_rcp_f32_e32 v250, v250
	v_mul_f32_e32 v232, v232, v243
	v_mul_f32_e32 v233, v233, v244
	v_mul_f32_e32 v234, v234, v245
	v_mul_f32_e32 v235, v235, v246
	v_mul_f32_e32 v236, v236, v247
	v_mul_f32_e32 v237, v237, v248
	v_mul_f32_e32 v238, v238, v249
	v_mul_f32_e32 v239, v239, v250
	v_mul_f32_e32 v232, v202, v232
	v_mul_f32_e32 v233, v203, v233
	v_mul_f32_e32 v234, v204, v234
	v_mul_f32_e32 v235, v205, v235
	v_mul_f32_e32 v236, v206, v236
	v_mul_f32_e32 v237, v207, v237
	v_mul_f32_e32 v238, v208, v238
	v_mul_f32_e32 v239, v209, v239
	v_mov_b32_e32 v212, 0
	v_mov_b32_e32 v213, 0
	v_cvt_pk_fp8_f32 v212, v232, v233
	v_cvt_pk_fp8_f32 v213, v236, v237
	v_cvt_pk_fp8_f32 v212, v234, v235 op_sel:[0,0,1]
	v_cvt_pk_fp8_f32 v213, v238, v239 op_sel:[0,0,1]
	v_add_co_u32_e32 v24, vcc, 0x18000, v18
	s_nop 1
	v_addc_co_u32_e32 v25, vcc, 0, v19, vcc
	global_store_dwordx2 v[24:25], v[212:213], off
	v_add_f32_e32 v232, v114, v14
	v_add_f32_e32 v233, v115, v16
	v_add_f32_e32 v234, v116, v10
	v_add_f32_e32 v235, v117, v12
	v_add_f32_e32 v236, v110, v6
	v_add_f32_e32 v237, v111, v8
	v_add_f32_e32 v238, v112, v2
	v_add_f32_e32 v239, v113, v4
	v_min_f32_e32 v232, 0x40e00000, v232
	v_min_f32_e32 v233, 0x40e00000, v233
	v_min_f32_e32 v234, 0x40e00000, v234
	v_min_f32_e32 v235, 0x40e00000, v235
	v_min_f32_e32 v236, 0x40e00000, v236
	v_min_f32_e32 v237, 0x40e00000, v237
	v_min_f32_e32 v238, 0x40e00000, v238
	v_min_f32_e32 v239, 0x40e00000, v239
	v_mul_f32_e32 v243, 0xc01d265f, v232
	v_mul_f32_e32 v244, 0xc01d265f, v233
	v_mul_f32_e32 v245, 0xc01d265f, v234
	v_mul_f32_e32 v246, 0xc01d265f, v235
	v_mul_f32_e32 v247, 0xc01d265f, v236
	v_mul_f32_e32 v248, 0xc01d265f, v237
	v_mul_f32_e32 v249, 0xc01d265f, v238
	v_mul_f32_e32 v250, 0xc01d265f, v239
	v_exp_f32_e32 v243, v243
	v_exp_f32_e32 v244, v244
	v_exp_f32_e32 v245, v245
	v_exp_f32_e32 v246, v246
	v_exp_f32_e32 v247, v247
	v_exp_f32_e32 v248, v248
	v_exp_f32_e32 v249, v249
	v_exp_f32_e32 v250, v250
	v_add_f32_e32 v202, v82, v15
	v_add_f32_e32 v203, v83, v17
	v_add_f32_e32 v204, v84, v11
	v_add_f32_e32 v205, v85, v13
	v_add_f32_e32 v206, v78, v7
	v_add_f32_e32 v207, v79, v9
	v_add_f32_e32 v208, v80, v3
	v_add_f32_e32 v209, v81, v5
	v_med3_f32 v202, v202, s86, v228
	v_med3_f32 v203, v203, s86, v228
	v_med3_f32 v204, v204, s86, v228
	v_med3_f32 v205, v205, s86, v228
	v_med3_f32 v206, v206, s86, v228
	v_med3_f32 v207, v207, s86, v228
	v_med3_f32 v208, v208, s86, v228
	v_med3_f32 v209, v209, s86, v228
	v_add_f32_e32 v243, 1.0, v243
	v_add_f32_e32 v244, 1.0, v244
	v_add_f32_e32 v245, 1.0, v245
	v_add_f32_e32 v246, 1.0, v246
	v_add_f32_e32 v247, 1.0, v247
	v_add_f32_e32 v248, 1.0, v248
	v_add_f32_e32 v249, 1.0, v249
	v_add_f32_e32 v250, 1.0, v250
	v_rcp_f32_e32 v243, v243
	v_rcp_f32_e32 v244, v244
	v_rcp_f32_e32 v245, v245
	v_rcp_f32_e32 v246, v246
	v_rcp_f32_e32 v247, v247
	v_rcp_f32_e32 v248, v248
	v_rcp_f32_e32 v249, v249
	v_rcp_f32_e32 v250, v250
	v_mul_f32_e32 v232, v232, v243
	v_mul_f32_e32 v233, v233, v244
	v_mul_f32_e32 v234, v234, v245
	v_mul_f32_e32 v235, v235, v246
	v_mul_f32_e32 v236, v236, v247
	v_mul_f32_e32 v237, v237, v248
	v_mul_f32_e32 v238, v238, v249
	v_mul_f32_e32 v239, v239, v250
	v_mul_f32_e32 v232, v202, v232
	v_mul_f32_e32 v233, v203, v233
	v_mul_f32_e32 v234, v204, v234
	v_mul_f32_e32 v235, v205, v235
	v_mul_f32_e32 v236, v206, v236
	v_mul_f32_e32 v237, v207, v237
	v_mul_f32_e32 v238, v208, v238
	v_mul_f32_e32 v239, v209, v239
	v_mov_b32_e32 v210, 0
	v_mov_b32_e32 v211, 0
	v_cvt_pk_fp8_f32 v210, v232, v233
	v_cvt_pk_fp8_f32 v211, v236, v237
	v_cvt_pk_fp8_f32 v210, v234, v235 op_sel:[0,0,1]
	v_cvt_pk_fp8_f32 v211, v238, v239 op_sel:[0,0,1]
	v_add_co_u32_e32 v24, vcc, 0x40000, v18
	s_nop 1
	v_addc_co_u32_e32 v25, vcc, 0, v19, vcc
	global_store_dwordx2 v[24:25], v[210:211], off
	v_add_f32_e32 v232, v106, v14
	v_add_f32_e32 v233, v107, v16
	v_add_f32_e32 v234, v108, v10
	v_add_f32_e32 v235, v109, v12
	v_add_f32_e32 v236, v102, v6
	v_add_f32_e32 v237, v103, v8
	v_add_f32_e32 v238, v104, v2
	v_add_f32_e32 v239, v105, v4
	v_min_f32_e32 v232, 0x40e00000, v232
	v_min_f32_e32 v233, 0x40e00000, v233
	v_min_f32_e32 v234, 0x40e00000, v234
	v_min_f32_e32 v235, 0x40e00000, v235
	v_min_f32_e32 v236, 0x40e00000, v236
	v_min_f32_e32 v237, 0x40e00000, v237
	v_min_f32_e32 v238, 0x40e00000, v238
	v_min_f32_e32 v239, 0x40e00000, v239
	v_mul_f32_e32 v243, 0xc01d265f, v232
	v_mul_f32_e32 v244, 0xc01d265f, v233
	v_mul_f32_e32 v245, 0xc01d265f, v234
	v_mul_f32_e32 v246, 0xc01d265f, v235
	v_mul_f32_e32 v247, 0xc01d265f, v236
	v_mul_f32_e32 v248, 0xc01d265f, v237
	v_mul_f32_e32 v249, 0xc01d265f, v238
	v_mul_f32_e32 v250, 0xc01d265f, v239
	v_exp_f32_e32 v243, v243
	v_exp_f32_e32 v244, v244
	v_exp_f32_e32 v245, v245
	v_exp_f32_e32 v246, v246
	v_exp_f32_e32 v247, v247
	v_exp_f32_e32 v248, v248
	v_exp_f32_e32 v249, v249
	v_exp_f32_e32 v250, v250
	v_add_f32_e32 v202, v74, v15
	v_add_f32_e32 v203, v75, v17
	v_add_f32_e32 v204, v76, v11
	v_add_f32_e32 v205, v77, v13
	v_add_f32_e32 v206, v70, v7
	v_add_f32_e32 v207, v71, v9
	v_add_f32_e32 v208, v72, v3
	v_add_f32_e32 v209, v73, v5
	v_med3_f32 v202, v202, s86, v228
	v_med3_f32 v203, v203, s86, v228
	v_med3_f32 v204, v204, s86, v228
	v_med3_f32 v205, v205, s86, v228
	v_med3_f32 v206, v206, s86, v228
	v_med3_f32 v207, v207, s86, v228
	v_med3_f32 v208, v208, s86, v228
	v_med3_f32 v209, v209, s86, v228
	v_add_f32_e32 v243, 1.0, v243
	v_add_f32_e32 v244, 1.0, v244
	v_add_f32_e32 v245, 1.0, v245
	v_add_f32_e32 v246, 1.0, v246
	v_add_f32_e32 v247, 1.0, v247
	v_add_f32_e32 v248, 1.0, v248
; __device__ __forceinline__ unsigned pk4_fp8(float a, float b, float c, float d) { int w = 0; w = __builtin_amdgcn_cvt_pk_fp8_f32(a, b, w, false); w = __builtin_amdgcn_cvt_pk_fp8_f32(c, d, w, true); return (unsigned)w; }
;     __device__ __forceinline__ void operator()(const Acc& acc, const Unit& u, int wr, int wc, int fr, int fq) const {
;     ...
;             for (int m = 0; m < 4; ++m) { const int row = row0 + ai * 128 + m * 16; float o[8];
; #pragma unroll
;                 for (int j = 0; j < 8; ++j) { float g = acc[ai][0][m][j >> 2][j & 3] * (MOE1_FP6 ? 1.f : W8_INV) + bg[j], l = acc[ai][1][m][j >> 2][j & 3] * (MOE1_FP6 ? 1.f : W8_INV) + bl[j];
;                     g = fminf(g, 7.f); l = fminf(fmaxf(l, -6.f), 8.f);
;                     o[j] = g * __builtin_amdgcn_rcpf(1.f + __builtin_amdgcn_exp2f(-2.4554669595930156f * g)) * l; }
;                 if (MOE_FP8) { u32x2 w; w.x = pk4_fp8(o[0], o[1], o[2], o[3]); w.y = pk4_fp8(o[4], o[5], o[6], o[7]); *(u32x2*)((unsigned char*)dst + (size_t)row * DE + a0) = w; }
	v_add_f32_e32 v249, 1.0, v249
	v_add_f32_e32 v250, 1.0, v250
	v_rcp_f32_e32 v243, v243
	v_rcp_f32_e32 v244, v244
	v_rcp_f32_e32 v245, v245
	v_rcp_f32_e32 v246, v246
	v_rcp_f32_e32 v247, v247
	v_rcp_f32_e32 v248, v248
	v_rcp_f32_e32 v249, v249
	v_rcp_f32_e32 v250, v250
	v_mul_f32_e32 v232, v232, v243
	v_mul_f32_e32 v233, v233, v244
	v_mul_f32_e32 v234, v234, v245
	v_mul_f32_e32 v235, v235, v246
	v_mul_f32_e32 v236, v236, v247
	v_mul_f32_e32 v237, v237, v248
	v_mul_f32_e32 v238, v238, v249
	v_mul_f32_e32 v239, v239, v250
	v_mul_f32_e32 v232, v202, v232
	v_mul_f32_e32 v233, v203, v233
	v_mul_f32_e32 v234, v204, v234
	v_mul_f32_e32 v235, v205, v235
	v_mul_f32_e32 v236, v206, v236
	v_mul_f32_e32 v237, v207, v237
	v_mul_f32_e32 v238, v208, v238
	v_mul_f32_e32 v239, v209, v239
	v_mov_b32_e32 v212, 0
	v_mov_b32_e32 v213, 0
	v_cvt_pk_fp8_f32 v212, v232, v233
	v_cvt_pk_fp8_f32 v213, v236, v237
	v_cvt_pk_fp8_f32 v212, v234, v235 op_sel:[0,0,1]
	v_cvt_pk_fp8_f32 v213, v238, v239 op_sel:[0,0,1]
	v_add_co_u32_e32 v24, vcc, 0x48000, v18
	s_nop 1
	v_addc_co_u32_e32 v25, vcc, 0, v19, vcc
	global_store_dwordx2 v[24:25], v[212:213], off
	v_add_f32_e32 v232, v98, v14
	v_add_f32_e32 v233, v99, v16
	v_add_f32_e32 v234, v100, v10
	v_add_f32_e32 v235, v101, v12
	v_add_f32_e32 v236, v94, v6
	v_add_f32_e32 v237, v95, v8
	v_add_f32_e32 v238, v96, v2
	v_add_f32_e32 v239, v97, v4
	v_min_f32_e32 v232, 0x40e00000, v232
	v_min_f32_e32 v233, 0x40e00000, v233
	v_min_f32_e32 v234, 0x40e00000, v234
	v_min_f32_e32 v235, 0x40e00000, v235
	v_min_f32_e32 v236, 0x40e00000, v236
	v_min_f32_e32 v237, 0x40e00000, v237
	v_min_f32_e32 v238, 0x40e00000, v238
	v_min_f32_e32 v239, 0x40e00000, v239
	v_mul_f32_e32 v243, 0xc01d265f, v232
	v_mul_f32_e32 v244, 0xc01d265f, v233
	v_mul_f32_e32 v245, 0xc01d265f, v234
	v_mul_f32_e32 v246, 0xc01d265f, v235
	v_mul_f32_e32 v247, 0xc01d265f, v236
	v_mul_f32_e32 v248, 0xc01d265f, v237
	v_mul_f32_e32 v249, 0xc01d265f, v238
	v_mul_f32_e32 v250, 0xc01d265f, v239
	v_exp_f32_e32 v243, v243
	v_exp_f32_e32 v244, v244
	v_exp_f32_e32 v245, v245
	v_exp_f32_e32 v246, v246
	v_exp_f32_e32 v247, v247
	v_exp_f32_e32 v248, v248
	v_exp_f32_e32 v249, v249
	v_exp_f32_e32 v250, v250
	v_add_f32_e32 v202, v66, v15
	v_add_f32_e32 v203, v67, v17
	v_add_f32_e32 v204, v68, v11
	v_add_f32_e32 v205, v69, v13
	v_add_f32_e32 v206, v62, v7
	v_add_f32_e32 v207, v63, v9
	v_add_f32_e32 v208, v64, v3
	v_add_f32_e32 v209, v65, v5
	v_med3_f32 v202, v202, s86, v228
	v_med3_f32 v203, v203, s86, v228
	v_med3_f32 v204, v204, s86, v228
	v_med3_f32 v205, v205, s86, v228
	v_med3_f32 v206, v206, s86, v228
	v_med3_f32 v207, v207, s86, v228
	v_med3_f32 v208, v208, s86, v228
	v_med3_f32 v209, v209, s86, v228
	v_add_f32_e32 v243, 1.0, v243
	v_add_f32_e32 v244, 1.0, v244
	v_add_f32_e32 v245, 1.0, v245
	v_add_f32_e32 v246, 1.0, v246
	v_add_f32_e32 v247, 1.0, v247
	v_add_f32_e32 v248, 1.0, v248
	v_add_f32_e32 v249, 1.0, v249
	v_add_f32_e32 v250, 1.0, v250
	v_rcp_f32_e32 v243, v243
	v_rcp_f32_e32 v244, v244
	v_rcp_f32_e32 v245, v245
	v_rcp_f32_e32 v246, v246
	v_rcp_f32_e32 v247, v247
	v_rcp_f32_e32 v248, v248
	v_rcp_f32_e32 v249, v249
	v_rcp_f32_e32 v250, v250
	v_mul_f32_e32 v232, v232, v243
	v_mul_f32_e32 v233, v233, v244
	v_mul_f32_e32 v234, v234, v245
	v_mul_f32_e32 v235, v235, v246
	v_mul_f32_e32 v236, v236, v247
	v_mul_f32_e32 v237, v237, v248
	v_mul_f32_e32 v238, v238, v249
	v_mul_f32_e32 v239, v239, v250
	v_mul_f32_e32 v232, v202, v232
	v_mul_f32_e32 v233, v203, v233
	v_mul_f32_e32 v234, v204, v234
	v_mul_f32_e32 v235, v205, v235
	v_mul_f32_e32 v236, v206, v236
	v_mul_f32_e32 v237, v207, v237
	v_mul_f32_e32 v238, v208, v238
	v_mul_f32_e32 v239, v209, v239
	v_mov_b32_e32 v210, 0
	v_mov_b32_e32 v211, 0
	v_cvt_pk_fp8_f32 v210, v232, v233
	v_cvt_pk_fp8_f32 v211, v236, v237
	v_cvt_pk_fp8_f32 v210, v234, v235 op_sel:[0,0,1]
	v_cvt_pk_fp8_f32 v211, v238, v239 op_sel:[0,0,1]
	v_add_co_u32_e32 v24, vcc, 0x50000, v18
	s_nop 1
	v_addc_co_u32_e32 v25, vcc, 0, v19, vcc
	global_store_dwordx2 v[24:25], v[210:211], off
	v_add_f32_e32 v232, v90, v14
	v_add_f32_e32 v233, v91, v16
	v_add_f32_e32 v234, v92, v10
	v_add_f32_e32 v235, v93, v12
	v_add_f32_e32 v236, v86, v6
	v_add_f32_e32 v237, v87, v8
	v_add_f32_e32 v238, v88, v2
	v_add_f32_e32 v239, v89, v4
	v_min_f32_e32 v232, 0x40e00000, v232
	v_min_f32_e32 v233, 0x40e00000, v233
	v_min_f32_e32 v234, 0x40e00000, v234
	v_min_f32_e32 v235, 0x40e00000, v235
	v_min_f32_e32 v236, 0x40e00000, v236
	v_min_f32_e32 v237, 0x40e00000, v237
	v_min_f32_e32 v238, 0x40e00000, v238
	v_min_f32_e32 v239, 0x40e00000, v239
	v_mul_f32_e32 v243, 0xc01d265f, v232
	v_mul_f32_e32 v244, 0xc01d265f, v233
	v_mul_f32_e32 v245, 0xc01d265f, v234
	v_mul_f32_e32 v246, 0xc01d265f, v235
	v_mul_f32_e32 v247, 0xc01d265f, v236
	v_mul_f32_e32 v248, 0xc01d265f, v237
	v_mul_f32_e32 v249, 0xc01d265f, v238
	v_mul_f32_e32 v250, 0xc01d265f, v239
	v_exp_f32_e32 v243, v243
	v_exp_f32_e32 v244, v244
	v_exp_f32_e32 v245, v245
	v_exp_f32_e32 v246, v246
	v_exp_f32_e32 v247, v247
	v_exp_f32_e32 v248, v248
	v_exp_f32_e32 v249, v249
	v_exp_f32_e32 v250, v250
	v_add_f32_e32 v202, v58, v15
	v_add_f32_e32 v203, v59, v17
	v_add_f32_e32 v204, v60, v11
	v_add_f32_e32 v205, v61, v13
	v_add_f32_e32 v206, v54, v7
	v_add_f32_e32 v207, v55, v9
	v_add_f32_e32 v208, v56, v3
	v_add_f32_e32 v209, v57, v5
	v_med3_f32 v202, v202, s86, v228
	v_med3_f32 v203, v203, s86, v228
	v_med3_f32 v204, v204, s86, v228
	v_med3_f32 v205, v205, s86, v228
	v_med3_f32 v206, v206, s86, v228
	v_med3_f32 v207, v207, s86, v228
	v_med3_f32 v208, v208, s86, v228
	v_med3_f32 v209, v209, s86, v228
	v_add_f32_e32 v243, 1.0, v243
	v_add_f32_e32 v244, 1.0, v244
	v_add_f32_e32 v245, 1.0, v245
	v_add_f32_e32 v246, 1.0, v246
	v_add_f32_e32 v247, 1.0, v247
	v_add_f32_e32 v248, 1.0, v248
	v_add_f32_e32 v249, 1.0, v249
	v_add_f32_e32 v250, 1.0, v250
	v_rcp_f32_e32 v243, v243
	v_rcp_f32_e32 v244, v244
	v_rcp_f32_e32 v245, v245
	v_rcp_f32_e32 v246, v246
	v_rcp_f32_e32 v247, v247
	v_rcp_f32_e32 v248, v248
	v_rcp_f32_e32 v249, v249
	v_rcp_f32_e32 v250, v250
	v_mul_f32_e32 v232, v232, v243
	v_mul_f32_e32 v233, v233, v244
	v_mul_f32_e32 v234, v234, v245
	v_mul_f32_e32 v235, v235, v246
	v_mul_f32_e32 v236, v236, v247
	v_mul_f32_e32 v237, v237, v248
	v_mul_f32_e32 v238, v238, v249
	v_mul_f32_e32 v239, v239, v250
	v_mul_f32_e32 v232, v202, v232
	v_mul_f32_e32 v233, v203, v233
	v_mul_f32_e32 v234, v204, v234
	v_mul_f32_e32 v235, v205, v235
	v_mul_f32_e32 v236, v206, v236
	v_mul_f32_e32 v237, v207, v237
	v_mul_f32_e32 v238, v208, v238
	v_mul_f32_e32 v239, v209, v239
	v_mov_b32_e32 v212, 0
	v_mov_b32_e32 v213, 0
	v_cvt_pk_fp8_f32 v212, v232, v233
	v_cvt_pk_fp8_f32 v213, v236, v237
	v_cvt_pk_fp8_f32 v212, v234, v235 op_sel:[0,0,1]
	v_cvt_pk_fp8_f32 v213, v238, v239 op_sel:[0,0,1]
	v_add_co_u32_e32 v24, vcc, 0x58000, v18
	s_nop 1
	v_addc_co_u32_e32 v25, vcc, 0, v19, vcc
	global_store_dwordx2 v[24:25], v[212:213], off
	s_andn2_b64 vcc, exec, s[20:21]
	s_cbranch_vccnz .LBB0_1952
;     ...
; #pragma unroll
;         for (int a = 0; a < 2; ++a)
; #pragma unroll
;             for (int b = 0; b < 2; ++b)
; #pragma unroll
;                 for (int m = 0; m < 4; ++m)
; #pragma unroll
;                     for (int n = 0; n < 2; ++n) acc[a][b][m][n] = (f32x4){0.f, 0.f, 0.f, 0.f};
;         cur = nxt; cB = nB; ++ui;
	v_mov_b32_e32 v52, v50
	v_mov_b32_e32 v53, v50
	v_mov_b32_e32 v51, v50
	v_mov_b64_e32 v[56:57], v[52:53]
	v_mov_b64_e32 v[60:61], v[52:53]
	v_mov_b64_e32 v[64:65], v[52:53]
	v_mov_b64_e32 v[68:69], v[52:53]
	v_mov_b64_e32 v[72:73], v[52:53]
	v_mov_b64_e32 v[76:77], v[52:53]
	v_mov_b64_e32 v[80:81], v[52:53]
	v_mov_b64_e32 v[84:85], v[52:53]
	v_mov_b64_e32 v[88:89], v[52:53]
	v_mov_b64_e32 v[92:93], v[52:53]
	v_mov_b64_e32 v[96:97], v[52:53]
	v_mov_b64_e32 v[100:101], v[52:53]
	v_mov_b64_e32 v[104:105], v[52:53]
	v_mov_b64_e32 v[108:109], v[52:53]
	v_mov_b64_e32 v[112:113], v[52:53]
	v_mov_b64_e32 v[116:117], v[52:53]
	v_mov_b64_e32 v[120:121], v[52:53]
	v_mov_b64_e32 v[124:125], v[52:53]
	v_mov_b64_e32 v[128:129], v[52:53]
	v_mov_b64_e32 v[132:133], v[52:53]
	v_mov_b64_e32 v[136:137], v[52:53]
	v_mov_b64_e32 v[140:141], v[52:53]
	v_mov_b64_e32 v[144:145], v[52:53]
	v_mov_b64_e32 v[148:149], v[52:53]
	v_mov_b64_e32 v[152:153], v[52:53]
	v_mov_b64_e32 v[156:157], v[52:53]
	v_mov_b64_e32 v[160:161], v[52:53]
	v_mov_b64_e32 v[164:165], v[52:53]
	v_mov_b64_e32 v[168:169], v[52:53]
	v_mov_b64_e32 v[172:173], v[52:53]
	v_mov_b64_e32 v[176:177], v[52:53]
	v_mov_b64_e32 v[180:181], v[52:53]
	v_mov_b64_e32 v[54:55], v[50:51]
	v_mov_b64_e32 v[58:59], v[50:51]
	v_mov_b64_e32 v[62:63], v[50:51]
	v_mov_b64_e32 v[66:67], v[50:51]
	v_mov_b64_e32 v[70:71], v[50:51]
	v_mov_b64_e32 v[74:75], v[50:51]
	v_mov_b64_e32 v[78:79], v[50:51]
	v_mov_b64_e32 v[82:83], v[50:51]
	v_mov_b64_e32 v[86:87], v[50:51]
	v_mov_b64_e32 v[90:91], v[50:51]
	v_mov_b64_e32 v[94:95], v[50:51]
	v_mov_b64_e32 v[98:99], v[50:51]
	v_mov_b64_e32 v[102:103], v[50:51]
	v_mov_b64_e32 v[106:107], v[50:51]
	v_mov_b64_e32 v[110:111], v[50:51]
	v_mov_b64_e32 v[114:115], v[50:51]
	v_mov_b64_e32 v[118:119], v[50:51]
	v_mov_b64_e32 v[122:123], v[50:51]
	v_mov_b64_e32 v[126:127], v[50:51]
	v_mov_b64_e32 v[130:131], v[50:51]
	v_mov_b64_e32 v[134:135], v[50:51]
	v_mov_b64_e32 v[138:139], v[50:51]
	v_mov_b64_e32 v[142:143], v[50:51]
	v_mov_b64_e32 v[146:147], v[50:51]
	v_mov_b64_e32 v[150:151], v[50:51]
	v_mov_b64_e32 v[154:155], v[50:51]
	v_mov_b64_e32 v[158:159], v[50:51]
	v_mov_b64_e32 v[162:163], v[50:51]
	v_mov_b64_e32 v[166:167], v[50:51]
	v_mov_b64_e32 v[170:171], v[50:51]
	v_mov_b64_e32 v[174:175], v[50:51]
	v_mov_b64_e32 v[178:179], v[50:51]
	s_mov_b32 s43, s91
	s_mov_b32 s44, s87
	s_mov_b32 s50, s90
	s_mov_b64 s[6:7], s[26:27]
	s_mov_b32 s88, s89
	s_branch .LBB0_1952

; __global__ void __launch_bounds__(512, 2) mega(P p, int lo, int hi, int bar_idx) {
	.amdhsa_kernel _Z4mega1Piii
		.amdhsa_group_segment_fixed_size 0
		.amdhsa_private_segment_fixed_size 0
		.amdhsa_kernarg_size 448
		.amdhsa_user_sgpr_count 2
		.amdhsa_user_sgpr_dispatch_ptr 0
		.amdhsa_user_sgpr_queue_ptr 0
		.amdhsa_user_sgpr_kernarg_segment_ptr 1
		.amdhsa_user_sgpr_dispatch_id 0
		.amdhsa_user_sgpr_kernarg_preload_length 0
		.amdhsa_user_sgpr_kernarg_preload_offset 0
		.amdhsa_user_sgpr_private_segment_size 0
		.amdhsa_uses_dynamic_stack 0
		.amdhsa_enable_private_segment 0
		.amdhsa_system_sgpr_workgroup_id_x 1
		.amdhsa_system_sgpr_workgroup_id_y 0
		.amdhsa_system_sgpr_workgroup_id_z 0
		.amdhsa_system_sgpr_workgroup_info 0
		.amdhsa_system_vgpr_workitem_id 0
		.amdhsa_next_free_vgpr 256
		.amdhsa_next_free_sgpr 102
		.amdhsa_accum_offset 256
		.amdhsa_reserve_vcc 1
		.amdhsa_float_round_mode_32 0
		.amdhsa_float_round_mode_16_64 0
		.amdhsa_float_denorm_mode_32 3
		.amdhsa_float_denorm_mode_16_64 3
		.amdhsa_dx10_clamp 1
		.amdhsa_ieee_mode 1
		.amdhsa_fp16_overflow 0
		.amdhsa_tg_split 0
		.amdhsa_exception_fp_ieee_invalid_op 0
		.amdhsa_exception_fp_denorm_src 0
		.amdhsa_exception_fp_ieee_div_zero 0
		.amdhsa_exception_fp_ieee_overflow 0
		.amdhsa_exception_fp_ieee_underflow 0
		.amdhsa_exception_fp_ieee_inexact 0
		.amdhsa_exception_int_div_zero 0
	.end_amdhsa_kernel

; __global__ void __launch_bounds__(512, 2) mega(P p, int lo, int hi, int bar_idx) {
amdhsa.kernels:
  - .agpr_count:     0
    .args:
      - .offset:         0
        .size:           176
        .value_kind:     by_value
      - .offset:         176
        .size:           4
        .value_kind:     by_value
      - .offset:         180
        .size:           4
        .value_kind:     by_value
      - .offset:         184
        .size:           4
        .value_kind:     by_value
      - .offset:         192
        .size:           4
        .value_kind:     hidden_block_count_x
      - .offset:         196
        .size:           4
        .value_kind:     hidden_block_count_y
      - .offset:         200
        .size:           4
        .value_kind:     hidden_block_count_z
      - .offset:         204
        .size:           2
        .value_kind:     hidden_group_size_x
      - .offset:         206
        .size:           2
        .value_kind:     hidden_group_size_y
      - .offset:         208
        .size:           2
        .value_kind:     hidden_group_size_z
      - .offset:         210
        .size:           2
        .value_kind:     hidden_remainder_x
      - .offset:         212
        .size:           2
        .value_kind:     hidden_remainder_y
      - .offset:         214
        .size:           2
        .value_kind:     hidden_remainder_z
      - .offset:         232
        .size:           8
        .value_kind:     hidden_global_offset_x
      - .offset:         240
        .size:           8
        .value_kind:     hidden_global_offset_y
      - .offset:         248
        .size:           8
        .value_kind:     hidden_global_offset_z
      - .offset:         256
        .size:           2
        .value_kind:     hidden_grid_dims
      - .offset:         312
        .size:           4
        .value_kind:     hidden_dynamic_lds_size
    .group_segment_fixed_size: 0
    .kernarg_segment_align: 8
    .kernarg_segment_size: 448
    .language:       OpenCL C
    .language_version:
      - 2
      - 0
    .max_flat_workgroup_size: 512
    .name:           _Z4mega1Piii
    .private_segment_fixed_size: 0
    .sgpr_count:     108
    .sgpr_spill_count: 174
    .symbol:         _Z4mega1Piii.kd
    .uniform_work_group_size: 1
    .uses_dynamic_stack: false
    .vgpr_count:     256
    .vgpr_spill_count: 0
    .wavefront_size: 64
